# speedup vs baseline: 1.0000x; 1.0000x over previous
.Lfarslow_ret_pre:
	v_pk_add_f32 v[120:121], v[120:121], v[128:129]
	v_pk_add_f32 v[122:123], v[122:123], v[130:131]
	v_pk_add_f32 v[140:141], v[140:141], v[148:149]
	v_pk_add_f32 v[142:143], v[142:143], v[150:151]
	v_pk_add_f32 v[120:121], v[120:121], v[140:141]
	v_pk_add_f32 v[122:123], v[122:123], v[142:143]
	s_nop 1
	v_permlane32_swap_b32_e32 v120, v122
	v_permlane32_swap_b32_e32 v121, v123
	v_pk_add_f32 v[44:45], v[120:121], v[122:123]
	v_add_u32_e32 v138, 0xfffffe00, v138
	v_add_u32_e32 v139, 0xffffff00, v139
	v_add_u32_e32 v156, 0xfffffa00, v156
	v_lshl_add_u64 v[158:159], v[158:159], 0, s[2:3]
	s_mov_b32 s5, 15
	v_add_u32_sdwa v88, v116, v42 dst_sel:DWORD dst_unused:UNUSED_PAD src0_sel:DWORD src1_sel:WORD_0
	v_add_u32_sdwa v89, v116, v42 dst_sel:DWORD dst_unused:UNUSED_PAD src0_sel:DWORD src1_sel:WORD_1
	v_add_u32_sdwa v90, v116, v43 dst_sel:DWORD dst_unused:UNUSED_PAD src0_sel:DWORD src1_sel:WORD_0
	v_add_u32_sdwa v91, v116, v43 dst_sel:DWORD dst_unused:UNUSED_PAD src0_sel:DWORD src1_sel:WORD_1
	v_bfe_u32 v117, v41, 16, 7
	v_add_u32_sdwa v118, v116, v39 dst_sel:DWORD dst_unused:UNUSED_PAD src0_sel:DWORD src1_sel:WORD_0
	v_add_u32_sdwa v119, v116, v39 dst_sel:DWORD dst_unused:UNUSED_PAD src0_sel:DWORD src1_sel:WORD_1
	v_add_u32_sdwa v136, v116, v41 dst_sel:DWORD dst_unused:UNUSED_PAD src0_sel:DWORD src1_sel:WORD_0
	s_or_b32 s10, s4, s21
	s_and_b32 s10, s10, 0x700
	s_and_b32 s9, s4, 0xff
	s_cselect_b32 s24, 0, 0x700
	s_or_b32 s10, s10, s24
	s_mov_b32 s5, 15
	s_cmp_lg_u32 s10, 0
	s_cbranch_scc1 .Lit_As
.Lit_Af:
	ds_read_b64 v[68:69], v88
	ds_read_b64 v[70:71], v89
	ds_read_b64 v[72:73], v90
	ds_read_b64 v[74:75], v91
	v_add_u32_sdwa v92, v105, v52 dst_sel:DWORD dst_unused:UNUSED_PAD src0_sel:DWORD src1_sel:WORD_0
	v_add_u32_sdwa v93, v105, v52 dst_sel:DWORD dst_unused:UNUSED_PAD src0_sel:DWORD src1_sel:WORD_1
	v_add_u32_sdwa v106, v105, v53 dst_sel:DWORD dst_unused:UNUSED_PAD src0_sel:DWORD src1_sel:WORD_0
	v_add_u32_sdwa v107, v105, v53 dst_sel:DWORD dst_unused:UNUSED_PAD src0_sel:DWORD src1_sel:WORD_1
	v_add_u32_sdwa v108, v105, v54 dst_sel:DWORD dst_unused:UNUSED_PAD src0_sel:DWORD src1_sel:WORD_0
	v_add_u32_sdwa v109, v105, v54 dst_sel:DWORD dst_unused:UNUSED_PAD src0_sel:DWORD src1_sel:WORD_1
	v_add_u32_sdwa v88, v105, v55 dst_sel:DWORD dst_unused:UNUSED_PAD src0_sel:DWORD src1_sel:WORD_0
	v_add_u32_sdwa v89, v105, v55 dst_sel:DWORD dst_unused:UNUSED_PAD src0_sel:DWORD src1_sel:WORD_1
	ds_read_b128 v[120:123], v92
	ds_read_b128 v[124:127], v93
	ds_read_b128 v[128:131], v106
	ds_read_b128 v[132:135], v107
	ds_read_b128 v[140:143], v108
	ds_read_b128 v[144:147], v109
	ds_read_b128 v[148:151], v88
	ds_read_b128 v[152:155], v89
	s_waitcnt lgkmcnt(11)
	v_pk_add_f32 v[76:77], v[44:45], v[68:69]
	s_waitcnt lgkmcnt(9)
	v_pk_add_f32 v[78:79], v[70:71], v[72:73]
	s_waitcnt lgkmcnt(8)
	v_pk_add_f32 v[76:77], v[76:77], v[74:75]
	ds_read_b128 v[46:49], v138 offset:56896
	v_pk_add_f32 v[76:77], v[76:77], v[78:79]
	ds_read_b64 v[50:51], v139
	v_pk_mul_f32 v[78:79], v[40:41], v[76:77] op_sel_hi:[0,1]
	v_cmp_eq_u32_e64 s[6:7], 1, v117
	ds_write_b64 v137, v[78:79]
	ds_read2_b64 v[56:59], v156 offset1:2
	s_waitcnt lgkmcnt(3)
	ds_read_b64 v[82:83], v118
	ds_read_b64 v[84:85], v119
	ds_read_b64 v[86:87], v136
	v_pk_add_f32 v[120:121], v[120:121], v[124:125]
	v_pk_add_f32 v[122:123], v[122:123], v[126:127]
	v_pk_add_f32 v[128:129], v[128:129], v[132:133]
	v_pk_add_f32 v[130:131], v[130:131], v[134:135]
	v_pk_add_f32 v[140:141], v[140:141], v[144:145]
	v_pk_add_f32 v[142:143], v[142:143], v[146:147]
	v_pk_add_f32 v[148:149], v[148:149], v[152:153]
	v_pk_add_f32 v[150:151], v[150:151], v[154:155]
	v_pk_add_f32 v[120:121], v[120:121], v[128:129]
	v_pk_add_f32 v[122:123], v[122:123], v[130:131]
	v_pk_add_f32 v[140:141], v[140:141], v[148:149]
	v_pk_add_f32 v[142:143], v[142:143], v[150:151]
	v_pk_add_f32 v[120:121], v[120:121], v[140:141]
	v_pk_add_f32 v[122:123], v[122:123], v[142:143]
	v_add_u32_e32 v138, 0xfffffe00, v138
	v_add_u32_e32 v139, 0xffffff00, v139
	v_permlane32_swap_b32_e32 v120, v122
	v_permlane32_swap_b32_e32 v121, v123
	v_pk_add_f32 v[62:63], v[120:121], v[122:123]
	s_mov_b64 exec, s[6:7]
	s_waitcnt lgkmcnt(2)
	v_pk_fma_f32 v[80:81], v[40:41], v[82:83], v[78:79] op_sel_hi:[0,1,1]
	s_waitcnt lgkmcnt(1)
	v_pk_fma_f32 v[80:81], v[40:41], v[84:85], v[80:81] op_sel_hi:[0,1,1]
	s_waitcnt lgkmcnt(0)
	v_pk_fma_f32 v[80:81], v[40:41], v[86:87], v[80:81] op_sel_hi:[0,1,1]
	ds_write_b64 v137, v[80:81]
	s_mov_b64 exec, -1
	s_cmp_lt_u32 s9, 2
	s_cbranch_scc1 .Lnp_Af
	v_cmp_eq_u32_e64 s[6:7], 2, v117
	s_nop 0
	s_mov_b64 exec, s[6:7]
	ds_read_b64 v[82:83], v118
	ds_read_b64 v[84:85], v119
	ds_read_b64 v[86:87], v136
	s_mov_b64 exec, -1
	v_add_u32_sdwa v88, v116, v50 dst_sel:DWORD dst_unused:UNUSED_PAD src0_sel:DWORD src1_sel:WORD_0
	v_add_u32_sdwa v89, v116, v50 dst_sel:DWORD dst_unused:UNUSED_PAD src0_sel:DWORD src1_sel:WORD_1
	v_add_u32_sdwa v90, v116, v51 dst_sel:DWORD dst_unused:UNUSED_PAD src0_sel:DWORD src1_sel:WORD_0
	v_add_u32_sdwa v91, v116, v51 dst_sel:DWORD dst_unused:UNUSED_PAD src0_sel:DWORD src1_sel:WORD_1
	v_bfe_u32 v168, v49, 16, 7
	v_add_u32_sdwa v169, v116, v47 dst_sel:DWORD dst_unused:UNUSED_PAD src0_sel:DWORD src1_sel:WORD_0
	v_add_u32_sdwa v170, v116, v47 dst_sel:DWORD dst_unused:UNUSED_PAD src0_sel:DWORD src1_sel:WORD_1
	v_add_u32_sdwa v171, v116, v49 dst_sel:DWORD dst_unused:UNUSED_PAD src0_sel:DWORD src1_sel:WORD_0
	v_add_u32_e32 v156, 0xfffffa00, v156
	v_add_u32_e32 v172, 0xfffffe00, v137
	v_readlane_b32 s4, v60, s5
	v_max_i32_e32 v156, v156, v162
	v_lshl_add_u64 v[158:159], v[158:159], 0, s[2:3]
	s_or_b32 s10, s21, s4
	s_and_b32 s10, s10, 0x700
	s_and_b32 s23, s21, 0xff
	s_cselect_b32 s24, 0, 0x700
	s_or_b32 s10, s10, s24
	s_mov_b64 exec, s[6:7]
	s_waitcnt lgkmcnt(2)
	v_pk_fma_f32 v[80:81], v[40:41], v[82:83], v[78:79] op_sel_hi:[0,1,1]
	s_waitcnt lgkmcnt(1)
	v_pk_fma_f32 v[80:81], v[40:41], v[84:85], v[80:81] op_sel_hi:[0,1,1]
	s_waitcnt lgkmcnt(0)
	v_pk_fma_f32 v[80:81], v[40:41], v[86:87], v[80:81] op_sel_hi:[0,1,1]
	ds_write_b64 v137, v[80:81]
	s_mov_b64 exec, -1
	s_cmp_lt_u32 s9, 3
	s_cbranch_scc1 .Lbot_A
	s_mov_b32 s8, 3

.Lbot_A:
	s_sub_u32 s5, s5, 1
	s_cmp_lg_u32 s10, 0
	s_cbranch_scc1 .Lit_Bs
.Lit_Bf:
	ds_read_b64 v[68:69], v88
	ds_read_b64 v[70:71], v89
	ds_read_b64 v[72:73], v90
	ds_read_b64 v[74:75], v91
	v_add_u32_sdwa v92, v105, v56 dst_sel:DWORD dst_unused:UNUSED_PAD src0_sel:DWORD src1_sel:WORD_0
	v_add_u32_sdwa v93, v105, v56 dst_sel:DWORD dst_unused:UNUSED_PAD src0_sel:DWORD src1_sel:WORD_1
	v_add_u32_sdwa v106, v105, v57 dst_sel:DWORD dst_unused:UNUSED_PAD src0_sel:DWORD src1_sel:WORD_0
	v_add_u32_sdwa v107, v105, v57 dst_sel:DWORD dst_unused:UNUSED_PAD src0_sel:DWORD src1_sel:WORD_1
	v_add_u32_sdwa v108, v105, v58 dst_sel:DWORD dst_unused:UNUSED_PAD src0_sel:DWORD src1_sel:WORD_0
	v_add_u32_sdwa v109, v105, v58 dst_sel:DWORD dst_unused:UNUSED_PAD src0_sel:DWORD src1_sel:WORD_1
	v_add_u32_sdwa v88, v105, v59 dst_sel:DWORD dst_unused:UNUSED_PAD src0_sel:DWORD src1_sel:WORD_0
	v_add_u32_sdwa v89, v105, v59 dst_sel:DWORD dst_unused:UNUSED_PAD src0_sel:DWORD src1_sel:WORD_1
	ds_read_b128 v[120:123], v92
	ds_read_b128 v[124:127], v93
	ds_read_b128 v[128:131], v106
	ds_read_b128 v[132:135], v107
	ds_read_b128 v[140:143], v108
	ds_read_b128 v[144:147], v109
	ds_read_b128 v[148:151], v88
	ds_read_b128 v[152:155], v89
	s_waitcnt lgkmcnt(11)
	v_pk_add_f32 v[76:77], v[62:63], v[68:69]
	s_waitcnt lgkmcnt(9)
	v_pk_add_f32 v[78:79], v[70:71], v[72:73]
	s_waitcnt lgkmcnt(8)
	v_pk_add_f32 v[76:77], v[76:77], v[74:75]
	ds_read_b128 v[38:41], v138 offset:56896
	v_pk_add_f32 v[76:77], v[76:77], v[78:79]
	ds_read_b64 v[42:43], v139
	v_pk_mul_f32 v[78:79], v[48:49], v[76:77] op_sel_hi:[0,1]
	v_cmp_eq_u32_e64 s[6:7], 1, v168
	ds_write_b64 v172, v[78:79]
	ds_read2_b64 v[52:55], v156 offset1:2
	s_waitcnt lgkmcnt(3)
	ds_read_b64 v[82:83], v169
	ds_read_b64 v[84:85], v170
	ds_read_b64 v[86:87], v171
	v_pk_add_f32 v[120:121], v[120:121], v[124:125]
	v_pk_add_f32 v[122:123], v[122:123], v[126:127]
	v_pk_add_f32 v[128:129], v[128:129], v[132:133]
	v_pk_add_f32 v[130:131], v[130:131], v[134:135]
	v_pk_add_f32 v[140:141], v[140:141], v[144:145]
	v_pk_add_f32 v[142:143], v[142:143], v[146:147]
	v_pk_add_f32 v[148:149], v[148:149], v[152:153]
	v_pk_add_f32 v[150:151], v[150:151], v[154:155]
	v_pk_add_f32 v[120:121], v[120:121], v[128:129]
	v_pk_add_f32 v[122:123], v[122:123], v[130:131]
	v_pk_add_f32 v[140:141], v[140:141], v[148:149]
	v_pk_add_f32 v[142:143], v[142:143], v[150:151]
	v_pk_add_f32 v[120:121], v[120:121], v[140:141]
	v_pk_add_f32 v[122:123], v[122:123], v[142:143]
	v_add_u32_e32 v138, 0xfffffe00, v138
	v_add_u32_e32 v139, 0xffffff00, v139
	v_permlane32_swap_b32_e32 v120, v122
	v_permlane32_swap_b32_e32 v121, v123
	v_pk_add_f32 v[44:45], v[120:121], v[122:123]
	s_mov_b64 exec, s[6:7]
	s_waitcnt lgkmcnt(2)
	v_pk_fma_f32 v[80:81], v[48:49], v[82:83], v[78:79] op_sel_hi:[0,1,1]
	s_waitcnt lgkmcnt(1)
	v_pk_fma_f32 v[80:81], v[48:49], v[84:85], v[80:81] op_sel_hi:[0,1,1]
	s_waitcnt lgkmcnt(0)
	v_pk_fma_f32 v[80:81], v[48:49], v[86:87], v[80:81] op_sel_hi:[0,1,1]
	ds_write_b64 v172, v[80:81]
	s_mov_b64 exec, -1
	s_cmp_lt_u32 s23, 2
	s_cbranch_scc1 .Lnp_Bf
	v_cmp_eq_u32_e64 s[6:7], 2, v168
	s_nop 0
	s_mov_b64 exec, s[6:7]
	ds_read_b64 v[82:83], v169
	ds_read_b64 v[84:85], v170
	ds_read_b64 v[86:87], v171
	s_mov_b64 exec, -1
	v_add_u32_sdwa v88, v116, v42 dst_sel:DWORD dst_unused:UNUSED_PAD src0_sel:DWORD src1_sel:WORD_0
	v_add_u32_sdwa v89, v116, v42 dst_sel:DWORD dst_unused:UNUSED_PAD src0_sel:DWORD src1_sel:WORD_1
	v_add_u32_sdwa v90, v116, v43 dst_sel:DWORD dst_unused:UNUSED_PAD src0_sel:DWORD src1_sel:WORD_0
	v_add_u32_sdwa v91, v116, v43 dst_sel:DWORD dst_unused:UNUSED_PAD src0_sel:DWORD src1_sel:WORD_1
	v_bfe_u32 v117, v41, 16, 7
	v_add_u32_sdwa v118, v116, v39 dst_sel:DWORD dst_unused:UNUSED_PAD src0_sel:DWORD src1_sel:WORD_0
	v_add_u32_sdwa v119, v116, v39 dst_sel:DWORD dst_unused:UNUSED_PAD src0_sel:DWORD src1_sel:WORD_1
	v_add_u32_sdwa v136, v116, v41 dst_sel:DWORD dst_unused:UNUSED_PAD src0_sel:DWORD src1_sel:WORD_0
	v_add_u32_e32 v156, 0xfffffa00, v156
	v_add_u32_e32 v137, 0xfffffe00, v172
	v_readlane_b32 s21, v60, s5
	v_max_i32_e32 v156, v156, v162
	v_lshl_add_u64 v[158:159], v[158:159], 0, s[2:3]
	s_or_b32 s10, s4, s21
	s_and_b32 s10, s10, 0x700
	s_and_b32 s9, s4, 0xff
	s_cselect_b32 s24, 0, 0x700
	s_or_b32 s10, s10, s24
	s_mov_b64 exec, s[6:7]
	s_waitcnt lgkmcnt(2)
	v_pk_fma_f32 v[80:81], v[48:49], v[82:83], v[78:79] op_sel_hi:[0,1,1]
	s_waitcnt lgkmcnt(1)
	v_pk_fma_f32 v[80:81], v[48:49], v[84:85], v[80:81] op_sel_hi:[0,1,1]
	s_waitcnt lgkmcnt(0)
	v_pk_fma_f32 v[80:81], v[48:49], v[86:87], v[80:81] op_sel_hi:[0,1,1]
	ds_write_b64 v172, v[80:81]
	s_mov_b64 exec, -1
	s_cmp_lt_u32 s23, 3
	s_cbranch_scc1 .Lbot_B
	s_mov_b32 s8, 3
.Llev_Bf:
	v_cmp_eq_u32_e64 s[6:7], s8, v168
	s_add_u32 s8, s8, 1
	s_mov_b64 exec, s[6:7]
	ds_read_b64 v[82:83], v169
	ds_read_b64 v[84:85], v170
	ds_read_b64 v[86:87], v171
	s_waitcnt lgkmcnt(2)
	v_pk_fma_f32 v[80:81], v[48:49], v[82:83], v[78:79] op_sel_hi:[0,1,1]
	s_waitcnt lgkmcnt(1)
	v_pk_fma_f32 v[80:81], v[48:49], v[84:85], v[80:81] op_sel_hi:[0,1,1]
	s_waitcnt lgkmcnt(0)
	v_pk_fma_f32 v[80:81], v[48:49], v[86:87], v[80:81] op_sel_hi:[0,1,1]
	ds_write_b64 v172, v[80:81]
	s_mov_b64 exec, -1
	s_cmp_le_u32 s8, s23
	s_cbranch_scc1 .Llev_Bf
.Lbot_B:
	s_cmp_eq_u32 s5, 0
	s_cbranch_scc1 .Lchain_done
	s_sub_u32 s5, s5, 1
	s_cmp_lg_u32 s10, 0
	s_cbranch_scc0 .Lit_Af
.Lit_As:
	ds_read_b64 v[68:69], v88
	ds_read_b64 v[70:71], v89
	ds_read_b64 v[72:73], v90
	ds_read_b64 v[74:75], v91
	v_add_u32_sdwa v92, v105, v52 dst_sel:DWORD dst_unused:UNUSED_PAD src0_sel:DWORD src1_sel:WORD_0
	v_add_u32_sdwa v93, v105, v52 dst_sel:DWORD dst_unused:UNUSED_PAD src0_sel:DWORD src1_sel:WORD_1
	v_add_u32_sdwa v106, v105, v53 dst_sel:DWORD dst_unused:UNUSED_PAD src0_sel:DWORD src1_sel:WORD_0
	v_add_u32_sdwa v107, v105, v53 dst_sel:DWORD dst_unused:UNUSED_PAD src0_sel:DWORD src1_sel:WORD_1
	v_add_u32_sdwa v108, v105, v54 dst_sel:DWORD dst_unused:UNUSED_PAD src0_sel:DWORD src1_sel:WORD_0
	v_add_u32_sdwa v109, v105, v54 dst_sel:DWORD dst_unused:UNUSED_PAD src0_sel:DWORD src1_sel:WORD_1
	v_add_u32_sdwa v88, v105, v55 dst_sel:DWORD dst_unused:UNUSED_PAD src0_sel:DWORD src1_sel:WORD_0
	v_add_u32_sdwa v89, v105, v55 dst_sel:DWORD dst_unused:UNUSED_PAD src0_sel:DWORD src1_sel:WORD_1
	ds_read_b128 v[120:123], v92
	ds_read_b128 v[124:127], v93
	ds_read_b128 v[128:131], v106
	ds_read_b128 v[132:135], v107
	ds_read_b128 v[140:143], v108
	ds_read_b128 v[144:147], v109
	ds_read_b128 v[148:151], v88
	ds_read_b128 v[152:155], v89
	s_waitcnt lgkmcnt(11)
	v_pk_add_f32 v[76:77], v[44:45], v[68:69]
	s_waitcnt lgkmcnt(9)
	v_pk_add_f32 v[78:79], v[70:71], v[72:73]
	s_waitcnt lgkmcnt(8)
	v_pk_add_f32 v[76:77], v[76:77], v[74:75]
	ds_read_b128 v[46:49], v138 offset:56896
	v_pk_add_f32 v[76:77], v[76:77], v[78:79]
	ds_read_b64 v[50:51], v139
	s_bitcmp1_b32 s4, 10
	s_cbranch_scc1 .Lnearslow_As
.Lnearslow_ret_As:
	v_pk_mul_f32 v[78:79], v[40:41], v[76:77] op_sel_hi:[0,1]
	v_cmp_eq_u32_e64 s[6:7], 1, v117
	ds_write_b64 v137, v[78:79]
	ds_read2_b64 v[56:59], v156 offset1:2
	s_waitcnt lgkmcnt(3)
	s_bitcmp1_b32 s4, 9
	s_cbranch_scc1 .Lfs_As
	s_cmp_eq_u32 s9, 0
	s_cbranch_scc1 .Lfs_As
	ds_read_b64 v[82:83], v118
	ds_read_b64 v[84:85], v119
	ds_read_b64 v[86:87], v136

.Lslowend_As:
	s_waitcnt lgkmcnt(0)
	v_add_u32_sdwa v88, v116, v50 dst_sel:DWORD dst_unused:UNUSED_PAD src0_sel:DWORD src1_sel:WORD_0
	v_add_u32_sdwa v89, v116, v50 dst_sel:DWORD dst_unused:UNUSED_PAD src0_sel:DWORD src1_sel:WORD_1
	v_add_u32_sdwa v90, v116, v51 dst_sel:DWORD dst_unused:UNUSED_PAD src0_sel:DWORD src1_sel:WORD_0
	v_add_u32_sdwa v91, v116, v51 dst_sel:DWORD dst_unused:UNUSED_PAD src0_sel:DWORD src1_sel:WORD_1
	v_bfe_u32 v168, v49, 16, 7
	v_add_u32_sdwa v169, v116, v47 dst_sel:DWORD dst_unused:UNUSED_PAD src0_sel:DWORD src1_sel:WORD_0
	v_add_u32_sdwa v170, v116, v47 dst_sel:DWORD dst_unused:UNUSED_PAD src0_sel:DWORD src1_sel:WORD_1
	v_add_u32_sdwa v171, v116, v49 dst_sel:DWORD dst_unused:UNUSED_PAD src0_sel:DWORD src1_sel:WORD_0
	v_add_u32_e32 v156, 0xfffffa00, v156
	v_add_u32_e32 v172, 0xfffffe00, v137
	v_readlane_b32 s4, v60, s5
	v_max_i32_e32 v156, v156, v162
	v_lshl_add_u64 v[158:159], v[158:159], 0, s[2:3]
	s_or_b32 s10, s21, s4
	s_and_b32 s10, s10, 0x700
	s_and_b32 s23, s21, 0xff
	s_cselect_b32 s24, 0, 0x700
	s_or_b32 s10, s10, s24
	s_branch .Lbot_A
.Lit_Bs:
	ds_read_b64 v[68:69], v88
	ds_read_b64 v[70:71], v89
	ds_read_b64 v[72:73], v90
	ds_read_b64 v[74:75], v91
	v_add_u32_sdwa v92, v105, v56 dst_sel:DWORD dst_unused:UNUSED_PAD src0_sel:DWORD src1_sel:WORD_0
	v_add_u32_sdwa v93, v105, v56 dst_sel:DWORD dst_unused:UNUSED_PAD src0_sel:DWORD src1_sel:WORD_1
	v_add_u32_sdwa v106, v105, v57 dst_sel:DWORD dst_unused:UNUSED_PAD src0_sel:DWORD src1_sel:WORD_0
	v_add_u32_sdwa v107, v105, v57 dst_sel:DWORD dst_unused:UNUSED_PAD src0_sel:DWORD src1_sel:WORD_1
	v_add_u32_sdwa v108, v105, v58 dst_sel:DWORD dst_unused:UNUSED_PAD src0_sel:DWORD src1_sel:WORD_0
	v_add_u32_sdwa v109, v105, v58 dst_sel:DWORD dst_unused:UNUSED_PAD src0_sel:DWORD src1_sel:WORD_1
	v_add_u32_sdwa v88, v105, v59 dst_sel:DWORD dst_unused:UNUSED_PAD src0_sel:DWORD src1_sel:WORD_0
	v_add_u32_sdwa v89, v105, v59 dst_sel:DWORD dst_unused:UNUSED_PAD src0_sel:DWORD src1_sel:WORD_1
	ds_read_b128 v[120:123], v92
	ds_read_b128 v[124:127], v93
	ds_read_b128 v[128:131], v106
	ds_read_b128 v[132:135], v107
	ds_read_b128 v[140:143], v108
	ds_read_b128 v[144:147], v109
	ds_read_b128 v[148:151], v88
	ds_read_b128 v[152:155], v89
	s_waitcnt lgkmcnt(11)
	v_pk_add_f32 v[76:77], v[62:63], v[68:69]
	s_waitcnt lgkmcnt(9)
	v_pk_add_f32 v[78:79], v[70:71], v[72:73]
	s_waitcnt lgkmcnt(8)
	v_pk_add_f32 v[76:77], v[76:77], v[74:75]
	ds_read_b128 v[38:41], v138 offset:56896
	v_pk_add_f32 v[76:77], v[76:77], v[78:79]
	ds_read_b64 v[42:43], v139
	s_bitcmp1_b32 s21, 10
	s_cbranch_scc1 .Lnearslow_Bs
.Lnearslow_ret_Bs:
	v_pk_mul_f32 v[78:79], v[48:49], v[76:77] op_sel_hi:[0,1]
	v_cmp_eq_u32_e64 s[6:7], 1, v168
	ds_write_b64 v172, v[78:79]
	ds_read2_b64 v[52:55], v156 offset1:2
	s_waitcnt lgkmcnt(3)
	s_bitcmp1_b32 s21, 9
	s_cbranch_scc1 .Lfs_Bs
	s_cmp_eq_u32 s23, 0
	s_cbranch_scc1 .Lfs_Bs
	ds_read_b64 v[82:83], v169
	ds_read_b64 v[84:85], v170
	ds_read_b64 v[86:87], v171

.Lfarslow_ret_Bs:
	v_pk_add_f32 v[120:121], v[120:121], v[128:129]
	v_pk_add_f32 v[122:123], v[122:123], v[130:131]
	v_pk_add_f32 v[140:141], v[140:141], v[148:149]
	v_pk_add_f32 v[142:143], v[142:143], v[150:151]
	v_pk_add_f32 v[120:121], v[120:121], v[140:141]
	v_pk_add_f32 v[122:123], v[122:123], v[142:143]
	v_add_u32_e32 v138, 0xfffffe00, v138
	v_add_u32_e32 v139, 0xffffff00, v139
	v_permlane32_swap_b32_e32 v120, v122
	v_permlane32_swap_b32_e32 v121, v123
	v_pk_add_f32 v[44:45], v[120:121], v[122:123]
	s_bitcmp1_b32 s21, 9
	s_cbranch_scc1 .Lslowlev_Bs
	s_cmp_eq_u32 s23, 0
	s_cbranch_scc1 .Lslowend_Bs
	s_mov_b64 exec, s[6:7]
	s_waitcnt lgkmcnt(2)
	v_pk_fma_f32 v[80:81], v[48:49], v[82:83], v[78:79] op_sel_hi:[0,1,1]
	s_waitcnt lgkmcnt(1)
	v_pk_fma_f32 v[80:81], v[48:49], v[84:85], v[80:81] op_sel_hi:[0,1,1]
	s_waitcnt lgkmcnt(0)
	v_pk_fma_f32 v[80:81], v[48:49], v[86:87], v[80:81] op_sel_hi:[0,1,1]
	ds_write_b64 v172, v[80:81]
	s_mov_b64 exec, -1
	s_cmp_lt_u32 s23, 2
	s_cbranch_scc1 .Lslowend_Bs
	s_mov_b32 s8, 2

.Lslowend_Bs:
	s_waitcnt lgkmcnt(0)
	v_add_u32_sdwa v88, v116, v42 dst_sel:DWORD dst_unused:UNUSED_PAD src0_sel:DWORD src1_sel:WORD_0
	v_add_u32_sdwa v89, v116, v42 dst_sel:DWORD dst_unused:UNUSED_PAD src0_sel:DWORD src1_sel:WORD_1
	v_add_u32_sdwa v90, v116, v43 dst_sel:DWORD dst_unused:UNUSED_PAD src0_sel:DWORD src1_sel:WORD_0
	v_add_u32_sdwa v91, v116, v43 dst_sel:DWORD dst_unused:UNUSED_PAD src0_sel:DWORD src1_sel:WORD_1
	v_bfe_u32 v117, v41, 16, 7
	v_add_u32_sdwa v118, v116, v39 dst_sel:DWORD dst_unused:UNUSED_PAD src0_sel:DWORD src1_sel:WORD_0
	v_add_u32_sdwa v119, v116, v39 dst_sel:DWORD dst_unused:UNUSED_PAD src0_sel:DWORD src1_sel:WORD_1
	v_add_u32_sdwa v136, v116, v41 dst_sel:DWORD dst_unused:UNUSED_PAD src0_sel:DWORD src1_sel:WORD_0
	v_add_u32_e32 v156, 0xfffffa00, v156
	v_add_u32_e32 v137, 0xfffffe00, v172
	v_readlane_b32 s21, v60, s5
	v_max_i32_e32 v156, v156, v162
	v_lshl_add_u64 v[158:159], v[158:159], 0, s[2:3]
	s_or_b32 s10, s4, s21
	s_and_b32 s10, s10, 0x700
	s_and_b32 s9, s4, 0xff
	s_cselect_b32 s24, 0, 0x700
	s_or_b32 s10, s10, s24
	s_branch .Lbot_B
.Lnp_Af:
	v_add_u32_sdwa v88, v116, v50 dst_sel:DWORD dst_unused:UNUSED_PAD src0_sel:DWORD src1_sel:WORD_0
	v_add_u32_sdwa v89, v116, v50 dst_sel:DWORD dst_unused:UNUSED_PAD src0_sel:DWORD src1_sel:WORD_1
	v_add_u32_sdwa v90, v116, v51 dst_sel:DWORD dst_unused:UNUSED_PAD src0_sel:DWORD src1_sel:WORD_0
	v_add_u32_sdwa v91, v116, v51 dst_sel:DWORD dst_unused:UNUSED_PAD src0_sel:DWORD src1_sel:WORD_1
	v_bfe_u32 v168, v49, 16, 7
	v_add_u32_sdwa v169, v116, v47 dst_sel:DWORD dst_unused:UNUSED_PAD src0_sel:DWORD src1_sel:WORD_0
	v_add_u32_sdwa v170, v116, v47 dst_sel:DWORD dst_unused:UNUSED_PAD src0_sel:DWORD src1_sel:WORD_1
	v_add_u32_sdwa v171, v116, v49 dst_sel:DWORD dst_unused:UNUSED_PAD src0_sel:DWORD src1_sel:WORD_0
	v_add_u32_e32 v156, 0xfffffa00, v156
	v_add_u32_e32 v172, 0xfffffe00, v137
	v_readlane_b32 s4, v60, s5
	v_max_i32_e32 v156, v156, v162
	v_lshl_add_u64 v[158:159], v[158:159], 0, s[2:3]
	s_or_b32 s10, s21, s4
	s_and_b32 s10, s10, 0x700
	s_and_b32 s23, s21, 0xff
	s_cselect_b32 s24, 0, 0x700
	s_or_b32 s10, s10, s24
	s_branch .Lbot_A
.Lnp_Bf:
	v_add_u32_sdwa v88, v116, v42 dst_sel:DWORD dst_unused:UNUSED_PAD src0_sel:DWORD src1_sel:WORD_0
	v_add_u32_sdwa v89, v116, v42 dst_sel:DWORD dst_unused:UNUSED_PAD src0_sel:DWORD src1_sel:WORD_1
	v_add_u32_sdwa v90, v116, v43 dst_sel:DWORD dst_unused:UNUSED_PAD src0_sel:DWORD src1_sel:WORD_0
	v_add_u32_sdwa v91, v116, v43 dst_sel:DWORD dst_unused:UNUSED_PAD src0_sel:DWORD src1_sel:WORD_1
	v_bfe_u32 v117, v41, 16, 7
	v_add_u32_sdwa v118, v116, v39 dst_sel:DWORD dst_unused:UNUSED_PAD src0_sel:DWORD src1_sel:WORD_0
	v_add_u32_sdwa v119, v116, v39 dst_sel:DWORD dst_unused:UNUSED_PAD src0_sel:DWORD src1_sel:WORD_1
	v_add_u32_sdwa v136, v116, v41 dst_sel:DWORD dst_unused:UNUSED_PAD src0_sel:DWORD src1_sel:WORD_0
	v_add_u32_e32 v156, 0xfffffa00, v156
	v_add_u32_e32 v137, 0xfffffe00, v172
	v_readlane_b32 s21, v60, s5
	v_max_i32_e32 v156, v156, v162
	v_lshl_add_u64 v[158:159], v[158:159], 0, s[2:3]
	s_or_b32 s10, s4, s21
	s_and_b32 s10, s10, 0x700
	s_and_b32 s9, s4, 0xff
	s_cselect_b32 s24, 0, 0x700
	s_or_b32 s10, s10, s24
	s_branch .Lbot_B

.Lnearslow_Bs:
	v_sub_u32_e32 v164, v172, v116
	v_lshrrev_b32_e32 v164, 2, v164
	v_add_u32_e32 v164, 0x128c0, v164
	ds_read_b32 v165, v164
	v_lshlrev_b32_e32 v166, 4, v111
	v_sub_u32_e32 v166, v172, v166
	v_add_u32_e32 v166, 0x200, v166
	s_waitcnt lgkmcnt(0)
	v_cmp_ne_u32_e32 vcc, 0, v165
	s_and_saveexec_b64 s[12:13], vcc
	s_cbranch_execz .Lnearslow_end_Bs

.Lslowlev_Bs:
	s_waitcnt lgkmcnt(0)
	s_mov_b32 s8, 1
	v_sub_u32_e32 v164, v172, v116
	v_lshrrev_b32_e32 v164, 2, v164
	v_add_u32_e32 v164, 0x11040, v164
	v_lshlrev_b32_e32 v166, 4, v111
	v_sub_u32_e32 v166, v172, v166
	v_and_b32_e32 v165, 0x800000, v49
.Lsl_Bs:
	v_cmp_eq_u32_e64 s[6:7], s8, v168
	s_add_u32 s8, s8, 1
	s_mov_b64 exec, s[6:7]
	ds_read_b64 v[82:83], v169
	ds_read_b64 v[84:85], v170
	ds_read_b64 v[86:87], v171
	s_waitcnt lgkmcnt(2)
	v_pk_fma_f32 v[80:81], v[48:49], v[82:83], v[78:79] op_sel_hi:[0,1,1]
	s_waitcnt lgkmcnt(1)
	v_pk_fma_f32 v[80:81], v[48:49], v[84:85], v[80:81] op_sel_hi:[0,1,1]
	s_waitcnt lgkmcnt(0)
	v_pk_fma_f32 v[80:81], v[48:49], v[86:87], v[80:81] op_sel_hi:[0,1,1]
	v_cmp_ne_u32_e32 vcc, 0, v165
	s_and_saveexec_b64 s[12:13], vcc
	s_cbranch_execz .Lsl_w_Bs
	ds_read_b32 v167, v164
	s_waitcnt lgkmcnt(0)

.Lsl_w_Bs:
	s_mov_b64 exec, s[6:7]
	ds_write_b64 v172, v[80:81]
	s_mov_b64 exec, -1
	s_cmp_le_u32 s8, s23
	s_cbranch_scc1 .Lsl_Bs
	s_branch .Lslowend_Bs

	.amdhsa_kernel _Z8k3_chainPKfPK15HIP_vector_typeIiLj4EEPKtS6_S0_S0_Pf
		.amdhsa_group_segment_fixed_size 78016
		.amdhsa_private_segment_fixed_size 0
		.amdhsa_kernarg_size 56
		.amdhsa_user_sgpr_count 2
		.amdhsa_user_sgpr_dispatch_ptr 0
		.amdhsa_user_sgpr_queue_ptr 0
		.amdhsa_user_sgpr_kernarg_segment_ptr 1
		.amdhsa_user_sgpr_dispatch_id 0
		.amdhsa_user_sgpr_kernarg_preload_length 0
		.amdhsa_user_sgpr_kernarg_preload_offset 0
		.amdhsa_user_sgpr_private_segment_size 0
		.amdhsa_uses_dynamic_stack 0
		.amdhsa_enable_private_segment 0
		.amdhsa_system_sgpr_workgroup_id_x 1
		.amdhsa_system_sgpr_workgroup_id_y 0
		.amdhsa_system_sgpr_workgroup_id_z 0
		.amdhsa_system_sgpr_workgroup_info 0
		.amdhsa_system_vgpr_workitem_id 0
		.amdhsa_next_free_vgpr 177
		.amdhsa_next_free_sgpr 96
		.amdhsa_accum_offset 176
		.amdhsa_reserve_vcc 1
		.amdhsa_float_round_mode_32 0
		.amdhsa_float_round_mode_16_64 0
		.amdhsa_float_denorm_mode_32 3
		.amdhsa_float_denorm_mode_16_64 3
		.amdhsa_dx10_clamp 1
		.amdhsa_ieee_mode 1
		.amdhsa_fp16_overflow 0
		.amdhsa_tg_split 0
		.amdhsa_exception_fp_ieee_invalid_op 0
		.amdhsa_exception_fp_denorm_src 0
		.amdhsa_exception_fp_ieee_div_zero 0
		.amdhsa_exception_fp_ieee_overflow 0
		.amdhsa_exception_fp_ieee_underflow 0
		.amdhsa_exception_fp_ieee_inexact 0
		.amdhsa_exception_int_div_zero 0
	.end_amdhsa_kernel

amdhsa.kernels:
  - .agpr_count:     0
    .args:
      - .actual_access:  read_only
        .address_space:  global
        .offset:         0
        .size:           8
        .value_kind:     global_buffer
      - .actual_access:  read_only
        .address_space:  global
        .offset:         8
        .size:           8
        .value_kind:     global_buffer
      - .actual_access:  write_only
        .address_space:  global
        .offset:         16
        .size:           8
        .value_kind:     global_buffer
      - .actual_access:  write_only
        .address_space:  global
        .offset:         24
        .size:           8
        .value_kind:     global_buffer
      - .actual_access:  write_only
        .address_space:  global
        .offset:         32
        .size:           8
        .value_kind:     global_buffer
    .group_segment_fixed_size: 1024
    .kernarg_segment_align: 8
    .kernarg_segment_size: 40
    .language:       OpenCL C
    .language_version:
      - 2
      - 0
    .max_flat_workgroup_size: 256
    .name:           _Z7k1_packPKfS0_PmPiP15HIP_vector_typeIfLj4EE
    .private_segment_fixed_size: 0
    .sgpr_count:     16
    .sgpr_spill_count: 0
    .symbol:         _Z7k1_packPKfS0_PmPiP15HIP_vector_typeIfLj4EE.kd
    .uniform_work_group_size: 1
    .uses_dynamic_stack: false
    .vgpr_count:     33
    .vgpr_spill_count: 0
    .wavefront_size: 64
  - .agpr_count:     0
    .args:
      - .actual_access:  read_only
        .address_space:  global
        .offset:         0
        .size:           8
        .value_kind:     global_buffer
      - .actual_access:  read_only
        .address_space:  global
        .offset:         8
        .size:           8
        .value_kind:     global_buffer
      - .actual_access:  write_only
        .address_space:  global
        .offset:         16
        .size:           8
        .value_kind:     global_buffer
      - .actual_access:  read_only
        .address_space:  global
        .offset:         24
        .size:           8
        .value_kind:     global_buffer
      - .actual_access:  write_only
        .address_space:  global
        .offset:         32
        .size:           8
        .value_kind:     global_buffer
      - .actual_access:  write_only
        .address_space:  global
        .offset:         40
        .size:           8
        .value_kind:     global_buffer
      - .actual_access:  read_only
        .address_space:  global
        .offset:         48
        .size:           8
        .value_kind:     global_buffer
      - .address_space:  global
        .offset:         56
        .size:           8
        .value_kind:     global_buffer
      - .actual_access:  write_only
        .address_space:  global
        .offset:         64
        .size:           8
        .value_kind:     global_buffer
      - .actual_access:  write_only
        .address_space:  global
        .offset:         72
        .size:           8
        .value_kind:     global_buffer
    .group_segment_fixed_size: 34880
    .kernarg_segment_align: 8
    .kernarg_segment_size: 80
    .language:       OpenCL C
    .language_version:
      - 2
      - 0
    .max_flat_workgroup_size: 512
    .name:           _Z7k2_elimPKjPKiPiS2_PfP15HIP_vector_typeIiLj4EEPKfS4_PtSA_
    .private_segment_fixed_size: 0
    .sgpr_count:     50
    .sgpr_spill_count: 0
    .symbol:         _Z7k2_elimPKjPKiPiS2_PfP15HIP_vector_typeIiLj4EEPKfS4_PtSA_.kd
    .uniform_work_group_size: 1
    .uses_dynamic_stack: false
    .vgpr_count:     35
    .vgpr_spill_count: 0
    .wavefront_size: 64
  - .agpr_count:     0
    .args:
      - .actual_access:  read_only
        .address_space:  global
        .offset:         0
        .size:           8
        .value_kind:     global_buffer
      - .actual_access:  read_only
        .address_space:  global
        .offset:         8
        .size:           8
        .value_kind:     global_buffer
      - .actual_access:  read_only
        .address_space:  global
        .offset:         16
        .size:           8
        .value_kind:     global_buffer
      - .actual_access:  read_only
        .address_space:  global
        .offset:         24
        .size:           8
        .value_kind:     global_buffer
      - .actual_access:  read_only
        .address_space:  global
        .offset:         32
        .size:           8
        .value_kind:     global_buffer
      - .actual_access:  read_only
        .address_space:  global
        .offset:         40
        .size:           8
        .value_kind:     global_buffer
      - .actual_access:  write_only
        .address_space:  global
        .offset:         48
        .size:           8
        .value_kind:     global_buffer
    .group_segment_fixed_size: 78016
    .kernarg_segment_align: 8
    .kernarg_segment_size: 56
    .language:       OpenCL C
    .language_version:
      - 2
      - 0
    .max_flat_workgroup_size: 256
    .name:           _Z8k3_chainPKfPK15HIP_vector_typeIiLj4EEPKtS6_S0_S0_Pf
    .private_segment_fixed_size: 0
    .sgpr_count:     28
    .sgpr_spill_count: 0
    .symbol:         _Z8k3_chainPKfPK15HIP_vector_typeIiLj4EEPKtS6_S0_S0_Pf.kd
    .uniform_work_group_size: 1
    .uses_dynamic_stack: false
    .vgpr_count:     176
    .vgpr_spill_count: 0
    .wavefront_size: 64
